# diff attention near-diagonal tiles: score-bias ds_read2_b32 use offset0/offset1 immediates off one base, 15 v_add_u32 per block removed
# baseline (speedup 1.0000x reference)
.LBB0_189:
	s_add_i32 s44, s73, 0xfffffdb2
	s_cmp_gt_u32 s44, 0xfffffb44
	s_cselect_b64 s[42:43], -1, 0
	s_cmp_lt_u32 s44, 0xfffffb45
	s_cselect_b64 vcc, -1, 0
	s_cmp_gt_i32 s73, -1
	s_cselect_b64 s[44:45], -1, 0
	s_xor_b64 s[44:45], s[0:1], s[44:45]
	v_add_u32_e32 v212, s71, v243
	s_and_b64 s[44:45], vcc, s[44:45]
	v_add_u32_e32 v213, 0x21700, v212
	s_and_b64 vcc, exec, vcc
	s_cbranch_vccnz .LBB0_194
	ds_read2_b32 v[144:145], v213 offset1:1
	ds_read2_b32 v[160:161], v213 offset0:32 offset1:33
	ds_read2_b32 v[146:147], v213 offset0:2 offset1:3
	ds_read2_b32 v[162:163], v213 offset0:34 offset1:35
	ds_read2_b32 v[148:149], v213 offset0:8 offset1:9
	ds_read2_b32 v[164:165], v213 offset0:40 offset1:41
	ds_read2_b32 v[150:151], v213 offset0:10 offset1:11
	ds_read2_b32 v[166:167], v213 offset0:42 offset1:43
	ds_read2_b32 v[152:153], v213 offset0:16 offset1:17
	ds_read2_b32 v[168:169], v213 offset0:48 offset1:49
	ds_read2_b32 v[154:155], v213 offset0:18 offset1:19
	ds_read2_b32 v[170:171], v213 offset0:50 offset1:51
	ds_read2_b32 v[156:157], v213 offset0:24 offset1:25
	ds_read2_b32 v[172:173], v213 offset0:56 offset1:57
	ds_read2_b32 v[158:159], v213 offset0:26 offset1:27
	ds_read2_b32 v[174:175], v213 offset0:58 offset1:59
	s_branch .LBB0_195

.LBB0_195:
	v_add_u32_e32 v0, s49, v225
	v_add_u32_e32 v6, v0, v227
	v_add_u32_e32 v7, v0, v228
	ds_read_b128 v[244:247], v6
	ds_read_b128 v[248:251], v6 offset:8192
	ds_read_b128 v[236:239], v7
	ds_read_b128 v[208:211], v7 offset:8192
	v_add_u32_e32 v6, v0, v229
	v_add_u32_e32 v7, v0, v230
	ds_read_b128 v[2:5], v6
	ds_read_b128 v[8:11], v6 offset:8192
	ds_read_b128 v[12:15], v7
	s_xor_b64 s[44:45], s[44:45], -1
	v_add_u32_e32 v6, v0, v226
	s_waitcnt lgkmcnt(6)
	v_mfma_f32_32x32x16_bf16 v[144:159], v[244:247], v[176:179], v[144:159]
	ds_read_b128 v[244:247], v7 offset:8192
	s_waitcnt lgkmcnt(6)
	v_mfma_f32_32x32x16_bf16 v[160:175], v[248:251], v[176:179], v[160:175]
	s_waitcnt lgkmcnt(5)
	v_mfma_f32_32x32x16_bf16 v[144:159], v[236:239], v[180:183], v[144:159]
	ds_read_b128 v[248:251], v6
	ds_read_b128 v[236:239], v6 offset:8192
	s_waitcnt lgkmcnt(6)
	v_mfma_f32_32x32x16_bf16 v[160:175], v[208:211], v[180:183], v[160:175]
	v_add_u32_e32 v7, v0, v231
	s_waitcnt lgkmcnt(5)
	v_mfma_f32_32x32x16_bf16 v[144:159], v[2:5], v[184:187], v[144:159]
	s_waitcnt lgkmcnt(4)
	v_mfma_f32_32x32x16_bf16 v[160:175], v[8:11], v[184:187], v[160:175]
	s_waitcnt lgkmcnt(3)
	v_mfma_f32_32x32x16_bf16 v[144:159], v[12:15], v[188:191], v[144:159]
	s_waitcnt lgkmcnt(2)
	v_mfma_f32_32x32x16_bf16 v[160:175], v[244:247], v[188:191], v[160:175]
	ds_read_b128 v[244:247], v7
	s_nop 9
	v_exp_f32_e32 v6, v144
	v_exp_f32_e32 v3, v145
	v_exp_f32_e32 v10, v148
	v_exp_f32_e32 v11, v149
	v_exp_f32_e32 v12, v150
	v_exp_f32_e32 v148, v152
	v_exp_f32_e32 v150, v153
	v_exp_f32_e32 v156, v156
	v_exp_f32_e32 v157, v157
	v_exp_f32_e32 v5, v146
	v_exp_f32_e32 v152, v154
	v_exp_f32_e32 v158, v158
	v_exp_f32_e32 v8, v147
	v_exp_f32_e32 v13, v151
	v_exp_f32_e32 v154, v155
	v_exp_f32_e32 v159, v159
	v_exp_f32_e32 v2, v160
	v_exp_f32_e32 v144, v164
	v_exp_f32_e32 v149, v168
	v_exp_f32_e32 v160, v172
	v_exp_f32_e32 v4, v161
	v_exp_f32_e32 v145, v165
	v_exp_f32_e32 v151, v169
	v_exp_f32_e32 v161, v173
	v_add_f32_e32 v14, v6, v3
	v_add_f32_e32 v15, v10, v11
	v_add_f32_e32 v164, v148, v150
	v_add_f32_e32 v165, v156, v157
	v_exp_f32_e32 v7, v162
	v_exp_f32_e32 v146, v166
	v_exp_f32_e32 v153, v170
	v_exp_f32_e32 v162, v174
	v_add_f32_e32 v14, v5, v14
	v_add_f32_e32 v15, v12, v15
	v_add_f32_e32 v164, v152, v164
	v_add_f32_e32 v165, v158, v165
	v_exp_f32_e32 v9, v163
	v_exp_f32_e32 v147, v167
	v_exp_f32_e32 v155, v171
	v_exp_f32_e32 v163, v175
	v_add_f32_e32 v14, v8, v14
	v_add_f32_e32 v15, v13, v15
	v_add_f32_e32 v164, v154, v164
	v_add_f32_e32 v165, v159, v165
	v_add_f32_e32 v14, v2, v14
	v_add_f32_e32 v15, v144, v15
	v_add_f32_e32 v164, v149, v164
	v_add_f32_e32 v165, v160, v165
	v_add_f32_e32 v14, v4, v14
	v_add_f32_e32 v15, v145, v15
	v_add_f32_e32 v164, v151, v164
	v_add_f32_e32 v165, v161, v165
	v_add_f32_e32 v14, v7, v14
	v_add_f32_e32 v15, v146, v15
	v_add_f32_e32 v164, v153, v164
	v_add_f32_e32 v165, v162, v165
	v_add_f32_e32 v14, v9, v14
	v_add_f32_e32 v15, v147, v15
	v_add_f32_e32 v164, v155, v164
	v_add_f32_e32 v165, v163, v165
	v_add_f32_e32 v14, v14, v15
	v_add_f32_e32 v15, v164, v165
	v_add_f32_e32 v14, v14, v15
	v_mov_b32_e32 v15, v14
	v_cvt_pk_bf16_f32 v208, v6, v3
	v_cvt_pk_bf16_f32 v209, v5, v8
	v_cvt_pk_bf16_f32 v210, v10, v11
	v_cvt_pk_bf16_f32 v211, v12, v13
	v_cvt_pk_bf16_f32 v10, v148, v150
	v_cvt_pk_bf16_f32 v11, v152, v154
	v_cvt_pk_bf16_f32 v12, v156, v157
	v_cvt_pk_bf16_f32 v13, v158, v159
	v_cvt_pk_bf16_f32 v6, v2, v4
	v_cvt_pk_bf16_f32 v7, v7, v9
	v_cvt_pk_bf16_f32 v8, v144, v145
	v_cvt_pk_bf16_f32 v9, v146, v147
	v_cvt_pk_bf16_f32 v2, v149, v151
	v_cvt_pk_bf16_f32 v3, v153, v155
	v_cvt_pk_bf16_f32 v4, v160, v161
	v_cvt_pk_bf16_f32 v5, v162, v163
	v_permlane32_swap_b32_e32 v14, v15
	v_permlane32_swap_b32_e32 v208, v210
	v_permlane32_swap_b32_e32 v209, v211
	v_permlane32_swap_b32_e32 v10, v12
	v_permlane32_swap_b32_e32 v11, v13
	v_permlane32_swap_b32_e32 v6, v8
	v_permlane32_swap_b32_e32 v7, v9
	v_permlane32_swap_b32_e32 v2, v4
	v_permlane32_swap_b32_e32 v3, v5
	s_nop 15
	s_nop 15
	s_andn2_b64 vcc, exec, s[44:45]
	s_cbranch_vccnz .Lz_l1s1
	s_andn2_b64 vcc, exec, s[42:43]
	s_mov_b64 s[42:43], -1
	s_cbranch_vccnz .LBB0_198
	ds_read2_b32 v[160:161], v213 offset1:1
	ds_read2_b32 v[144:145], v213 offset0:32 offset1:33
	ds_read2_b32 v[162:163], v213 offset0:2 offset1:3
	ds_read2_b32 v[146:147], v213 offset0:34 offset1:35
	ds_read2_b32 v[164:165], v213 offset0:8 offset1:9
	ds_read2_b32 v[148:149], v213 offset0:40 offset1:41
	ds_read2_b32 v[166:167], v213 offset0:10 offset1:11
	ds_read2_b32 v[150:151], v213 offset0:42 offset1:43
	ds_read2_b32 v[168:169], v213 offset0:16 offset1:17
	ds_read2_b32 v[152:153], v213 offset0:48 offset1:49
	ds_read2_b32 v[170:171], v213 offset0:18 offset1:19
	ds_read2_b32 v[154:155], v213 offset0:50 offset1:51
	ds_read2_b32 v[172:173], v213 offset0:24 offset1:25
	ds_read2_b32 v[156:157], v213 offset0:56 offset1:57
	ds_read2_b32 v[174:175], v213 offset0:26 offset1:27
	ds_read2_b32 v[158:159], v213 offset0:58 offset1:59
	s_mov_b64 s[42:43], 0

.LBB0_210:
	s_add_i32 s44, s72, 0xfffffdb2
	s_cmp_gt_u32 s44, 0xfffffb44
	s_cselect_b64 s[42:43], -1, 0
	s_cmp_lt_u32 s44, 0xfffffb45
	s_cselect_b64 vcc, -1, 0
	s_cmp_gt_i32 s72, -1
	s_cselect_b64 s[44:45], -1, 0
	s_xor_b64 s[44:45], s[0:1], s[44:45]
	v_add_u32_e32 v219, s73, v0
	s_and_b64 s[44:45], vcc, s[44:45]
	v_add_u32_e32 v220, 0x21700, v219
	s_and_b64 vcc, exec, vcc
	s_cbranch_vccnz .LBB0_214
	ds_read2_b32 v[160:161], v220 offset1:1
	ds_read2_b32 v[144:145], v220 offset0:32 offset1:33
	ds_read2_b32 v[162:163], v220 offset0:2 offset1:3
	ds_read2_b32 v[146:147], v220 offset0:34 offset1:35
	ds_read2_b32 v[164:165], v220 offset0:8 offset1:9
	ds_read2_b32 v[148:149], v220 offset0:40 offset1:41
	ds_read2_b32 v[166:167], v220 offset0:10 offset1:11
	ds_read2_b32 v[150:151], v220 offset0:42 offset1:43
	ds_read2_b32 v[168:169], v220 offset0:16 offset1:17
	ds_read2_b32 v[152:153], v220 offset0:48 offset1:49
	ds_read2_b32 v[170:171], v220 offset0:18 offset1:19
	ds_read2_b32 v[154:155], v220 offset0:50 offset1:51
	ds_read2_b32 v[172:173], v220 offset0:24 offset1:25
	ds_read2_b32 v[156:157], v220 offset0:56 offset1:57
	ds_read2_b32 v[174:175], v220 offset0:26 offset1:27
	ds_read2_b32 v[158:159], v220 offset0:58 offset1:59
	s_branch .LBB0_215

.LBB0_215:
	v_add_u32_e32 v212, s56, v225
	v_add_u32_e32 v6, v212, v227
	v_add_u32_e32 v7, v212, v228
	ds_read_b128 v[244:247], v6
	ds_read_b128 v[248:251], v6 offset:8192
	ds_read_b128 v[236:239], v7
	ds_read_b128 v[240:243], v7 offset:8192
	v_add_u32_e32 v6, v212, v229
	v_add_u32_e32 v7, v212, v230
	ds_read_b128 v[2:5], v6
	ds_read_b128 v[8:11], v6 offset:8192
	ds_read_b128 v[208:211], v7
	s_xor_b64 s[44:45], s[44:45], -1
	v_add_u32_e32 v6, v212, v226
	s_waitcnt lgkmcnt(6)
	v_mfma_f32_32x32x16_bf16 v[160:175], v[244:247], v[176:179], v[160:175]
	ds_read_b128 v[244:247], v7 offset:8192
	s_waitcnt lgkmcnt(6)
	v_mfma_f32_32x32x16_bf16 v[144:159], v[248:251], v[176:179], v[144:159]
	s_waitcnt lgkmcnt(5)
	v_mfma_f32_32x32x16_bf16 v[160:175], v[236:239], v[180:183], v[160:175]
	v_add_u32_e32 v7, v212, v231
	s_waitcnt lgkmcnt(4)
	v_mfma_f32_32x32x16_bf16 v[144:159], v[240:243], v[180:183], v[144:159]
	ds_read_b128 v[248:251], v6
	ds_read_b128 v[236:239], v6 offset:8192
	ds_read_b128 v[240:243], v7
	s_waitcnt lgkmcnt(6)
	v_mfma_f32_32x32x16_bf16 v[160:175], v[2:5], v[184:187], v[160:175]
	s_waitcnt lgkmcnt(5)
	v_mfma_f32_32x32x16_bf16 v[144:159], v[8:11], v[184:187], v[144:159]
	s_waitcnt lgkmcnt(4)
	v_mfma_f32_32x32x16_bf16 v[160:175], v[208:211], v[188:191], v[160:175]
	s_waitcnt lgkmcnt(3)
	v_mfma_f32_32x32x16_bf16 v[144:159], v[244:247], v[188:191], v[144:159]
	ds_read_b128 v[244:247], v7 offset:8192
	s_nop 9
	v_exp_f32_e32 v6, v160
	v_exp_f32_e32 v3, v161
	v_exp_f32_e32 v10, v164
	v_exp_f32_e32 v11, v165
	v_exp_f32_e32 v160, v172
	v_exp_f32_e32 v161, v173
	v_exp_f32_e32 v5, v162
	v_exp_f32_e32 v2, v144
	v_exp_f32_e32 v7, v146
	v_exp_f32_e32 v144, v148
	v_exp_f32_e32 v146, v150
	v_exp_f32_e32 v148, v168
	v_exp_f32_e32 v150, v169
	v_exp_f32_e32 v4, v145
	v_exp_f32_e32 v145, v149
	v_exp_f32_e32 v12, v166
	v_exp_f32_e32 v149, v152
	v_exp_f32_e32 v152, v170
	v_exp_f32_e32 v162, v174
	v_exp_f32_e32 v8, v163
	v_exp_f32_e32 v9, v147
	v_exp_f32_e32 v13, v167
	v_exp_f32_e32 v147, v151
	v_exp_f32_e32 v151, v153
	v_exp_f32_e32 v153, v154
	v_exp_f32_e32 v154, v171
	v_exp_f32_e32 v163, v175
	v_exp_f32_e32 v156, v156
	v_exp_f32_e32 v157, v157
	v_add_f32_e32 v164, v6, v3
	v_add_f32_e32 v165, v10, v11
	v_add_f32_e32 v166, v148, v150
	v_add_f32_e32 v167, v160, v161
	v_exp_f32_e32 v158, v158
	v_add_f32_e32 v164, v5, v164
	v_add_f32_e32 v165, v12, v165
	v_add_f32_e32 v166, v152, v166
	v_add_f32_e32 v167, v162, v167
	v_exp_f32_e32 v155, v155
	v_exp_f32_e32 v159, v159
	v_add_f32_e32 v164, v8, v164
	v_add_f32_e32 v165, v13, v165
	v_add_f32_e32 v166, v154, v166
	v_add_f32_e32 v167, v163, v167
	v_add_f32_e32 v164, v2, v164
	v_add_f32_e32 v165, v144, v165
	v_add_f32_e32 v166, v149, v166
	v_add_f32_e32 v167, v156, v167
	v_add_f32_e32 v164, v4, v164
	v_add_f32_e32 v165, v145, v165
	v_add_f32_e32 v166, v151, v166
	v_add_f32_e32 v167, v157, v167
	v_add_f32_e32 v164, v7, v164
	v_add_f32_e32 v165, v146, v165
	v_add_f32_e32 v166, v153, v166
	v_add_f32_e32 v167, v158, v167
	v_add_f32_e32 v164, v9, v164
	v_add_f32_e32 v165, v147, v165
	v_add_f32_e32 v166, v155, v166
	v_add_f32_e32 v167, v159, v167
	v_add_f32_e32 v164, v164, v165
	v_add_f32_e32 v165, v166, v167
	v_add_f32_e32 v213, v164, v165
	v_mov_b32_e32 v218, v213
	v_cvt_pk_bf16_f32 v208, v6, v3
	v_cvt_pk_bf16_f32 v209, v5, v8
	v_cvt_pk_bf16_f32 v210, v10, v11
	v_cvt_pk_bf16_f32 v211, v12, v13
	v_cvt_pk_bf16_f32 v10, v148, v150
	v_cvt_pk_bf16_f32 v11, v152, v154
	v_cvt_pk_bf16_f32 v12, v160, v161
	v_cvt_pk_bf16_f32 v13, v162, v163
	v_cvt_pk_bf16_f32 v6, v2, v4
	v_cvt_pk_bf16_f32 v7, v7, v9
	v_cvt_pk_bf16_f32 v8, v144, v145
	v_cvt_pk_bf16_f32 v9, v146, v147
	v_cvt_pk_bf16_f32 v2, v149, v151
	v_cvt_pk_bf16_f32 v3, v153, v155
	v_cvt_pk_bf16_f32 v4, v156, v157
	v_cvt_pk_bf16_f32 v5, v158, v159
	v_permlane32_swap_b32_e32 v213, v218
	v_permlane32_swap_b32_e32 v208, v210
	v_permlane32_swap_b32_e32 v209, v211
	v_permlane32_swap_b32_e32 v10, v12
	v_permlane32_swap_b32_e32 v11, v13
	v_permlane32_swap_b32_e32 v6, v8
	v_permlane32_swap_b32_e32 v7, v9
	v_permlane32_swap_b32_e32 v2, v4
	v_permlane32_swap_b32_e32 v3, v5
	s_nop 15
	s_nop 15
	s_andn2_b64 vcc, exec, s[44:45]
	s_cbranch_vccnz .Lz_l2s1
	s_andn2_b64 vcc, exec, s[42:43]
	s_mov_b64 s[42:43], -1
	s_cbranch_vccnz .LBB0_218
	ds_read2_b32 v[144:145], v220 offset1:1
	ds_read2_b32 v[160:161], v220 offset0:32 offset1:33
	ds_read2_b32 v[146:147], v220 offset0:2 offset1:3
	ds_read2_b32 v[162:163], v220 offset0:34 offset1:35
	ds_read2_b32 v[148:149], v220 offset0:8 offset1:9
	ds_read2_b32 v[164:165], v220 offset0:40 offset1:41
	ds_read2_b32 v[150:151], v220 offset0:10 offset1:11
	ds_read2_b32 v[166:167], v220 offset0:42 offset1:43
	ds_read2_b32 v[152:153], v220 offset0:16 offset1:17
	ds_read2_b32 v[168:169], v220 offset0:48 offset1:49
	ds_read2_b32 v[154:155], v220 offset0:18 offset1:19
	ds_read2_b32 v[170:171], v220 offset0:50 offset1:51
	ds_read2_b32 v[156:157], v220 offset0:24 offset1:25
	ds_read2_b32 v[172:173], v220 offset0:56 offset1:57
	ds_read2_b32 v[158:159], v220 offset0:26 offset1:27
	ds_read2_b32 v[174:175], v220 offset0:58 offset1:59
	s_mov_b64 s[42:43], 0
